# first arriver of each XCD at a grid barrier issues an early L2 write-back so the leader's write-back finds less dirty data
# speedup vs baseline: 1.0076x; 1.0019x over previous
.LBB0_171:
	s_or_b64 exec, exec, s[8:9]
	v_cvt_f32_u32_e32 v4, v2
	s_waitcnt vmcnt(0)
	v_readfirstlane_b32 s4, v3
	v_sub_u32_e32 v3, 0, v2
	v_rcp_iflag_f32_e32 v4, v4
	v_add_u32_e32 v5, s4, v1
	v_mul_f32_e32 v4, 0x4f7ffffe, v4
	v_cvt_u32_f32_e32 v4, v4
	v_mul_lo_u32 v1, v3, v4
	v_mul_hi_u32 v1, v4, v1
	v_add_u32_e32 v1, v4, v1
	v_mul_hi_u32 v1, v5, v1
	v_mul_lo_u32 v3, v1, v2
	v_sub_u32_e32 v3, v5, v3
	v_add_u32_e32 v4, 1, v1
	v_cmp_ge_u32_e32 vcc, v3, v2
	s_nop 1
	v_cndmask_b32_e32 v1, v1, v4, vcc
	v_sub_u32_e32 v4, v3, v2
	v_cndmask_b32_e32 v3, v3, v4, vcc
	v_add_u32_e32 v4, 1, v1
	v_cmp_ge_u32_e32 vcc, v3, v2
	v_add_u32_e32 v3, 1, v5
	s_nop 0
	v_cndmask_b32_e32 v1, v1, v4, vcc
	v_mul_lo_u32 v4, v2, v1
	v_add_u32_e32 v2, v4, v2
	v_cmp_ne_u32_e32 vcc, v3, v2
	s_and_saveexec_b64 s[4:5], vcc
	s_xor_b64 s[6:7], exec, s[4:5]
	s_cbranch_execz .LBB0_185
	v_cmp_eq_u32_e32 vcc, v5, v4
	s_cbranch_vccz .Lfa_0
	buffer_wbl2 sc1
.Lfa_0:
	buffer_inv sc1
	s_waitcnt lgkmcnt(0)
	v_mov_b32_e32 v0, 0x2000
	global_load_dword v0, v0, s[2:3] offset:1024 sc1
	s_add_u32 s12, s2, 0x2400
	s_addc_u32 s13, s3, 0
	s_waitcnt vmcnt(0)
	v_cmp_eq_u32_e32 vcc, v0, v1
	s_and_saveexec_b64 s[8:9], vcc
	s_cbranch_execz .LBB0_184
	s_add_u32 s10, s46, 0x4200
	s_addc_u32 s11, s47, 0
	s_mov_b32 s4, 1
	s_mov_b64 s[14:15], 0
	v_mov_b32_e32 v0, 0
	s_branch .LBB0_175

.LBB0_289:
	s_or_b64 exec, exec, s[6:7]
	v_cvt_f32_u32_e32 v5, v3
	s_waitcnt vmcnt(0)
	v_readfirstlane_b32 s4, v4
	v_sub_u32_e32 v4, 0, v3
	v_rcp_iflag_f32_e32 v5, v5
	v_add_u32_e32 v6, s4, v0
	v_mul_f32_e32 v5, 0x4f7ffffe, v5
	v_cvt_u32_f32_e32 v5, v5
	v_mul_lo_u32 v0, v4, v5
	v_mul_hi_u32 v0, v5, v0
	v_add_u32_e32 v0, v5, v0
	v_mul_hi_u32 v0, v6, v0
	v_mul_lo_u32 v4, v0, v3
	v_sub_u32_e32 v4, v6, v4
	v_add_u32_e32 v5, 1, v0
	v_cmp_ge_u32_e32 vcc, v4, v3
	s_nop 1
	v_cndmask_b32_e32 v0, v0, v5, vcc
	v_sub_u32_e32 v5, v4, v3
	v_cndmask_b32_e32 v4, v4, v5, vcc
	v_add_u32_e32 v5, 1, v0
	v_cmp_ge_u32_e32 vcc, v4, v3
	v_add_u32_e32 v4, 1, v6
	s_nop 0
	v_cndmask_b32_e32 v0, v0, v5, vcc
	v_mul_lo_u32 v5, v3, v0
	v_add_u32_e32 v3, v5, v3
	v_cmp_ne_u32_e32 vcc, v4, v3
	s_and_saveexec_b64 s[4:5], vcc
	s_xor_b64 s[4:5], exec, s[4:5]
	s_cbranch_execz .LBB0_303
	v_cmp_eq_u32_e32 vcc, v6, v5
	s_cbranch_vccz .Lfa_4
	buffer_wbl2 sc1
.Lfa_4:
	buffer_inv sc1
	s_add_i32 s76, s9, 0x900
	s_lshl_b64 s[6:7], s[76:77], 2
	v_readlane_b32 s10, v254, 46
	v_readlane_b32 s11, v254, 47
	s_add_u32 s14, s10, s6
	s_addc_u32 s15, s11, s7
	s_waitcnt lgkmcnt(0)
	global_load_dword v2, v1, s[14:15] sc1
	s_waitcnt vmcnt(0)
	v_cmp_eq_u32_e32 vcc, v2, v0
	s_and_saveexec_b64 s[6:7], vcc
	s_cbranch_execz .LBB0_302
	s_mov_b32 s10, 1
	s_mov_b64 s[16:17], 0
	s_branch .LBB0_293

.LBB0_628:
	s_or_b64 exec, exec, s[6:7]
	v_cvt_f32_u32_e32 v5, v3
	s_waitcnt vmcnt(0)
	v_readfirstlane_b32 s2, v4
	v_sub_u32_e32 v4, 0, v3
	v_rcp_iflag_f32_e32 v5, v5
	v_add_u32_e32 v6, s2, v0
	v_mul_f32_e32 v5, 0x4f7ffffe, v5
	v_cvt_u32_f32_e32 v5, v5
	v_mul_lo_u32 v0, v4, v5
	v_mul_hi_u32 v0, v5, v0
	v_add_u32_e32 v0, v5, v0
	v_mul_hi_u32 v0, v6, v0
	v_mul_lo_u32 v4, v0, v3
	v_sub_u32_e32 v4, v6, v4
	v_add_u32_e32 v5, 1, v0
	v_cmp_ge_u32_e32 vcc, v4, v3
	s_nop 1
	v_cndmask_b32_e32 v0, v0, v5, vcc
	v_sub_u32_e32 v5, v4, v3
	v_cndmask_b32_e32 v4, v4, v5, vcc
	v_add_u32_e32 v5, 1, v0
	v_cmp_ge_u32_e32 vcc, v4, v3
	v_add_u32_e32 v4, 1, v6
	s_nop 0
	v_cndmask_b32_e32 v0, v0, v5, vcc
	v_mul_lo_u32 v5, v3, v0
	v_add_u32_e32 v3, v5, v3
	v_cmp_ne_u32_e32 vcc, v4, v3
	s_and_saveexec_b64 s[2:3], vcc
	s_xor_b64 s[2:3], exec, s[2:3]
	s_cbranch_execz .LBB0_642
	v_cmp_eq_u32_e32 vcc, v6, v5
	s_cbranch_vccz .Lfa_8
	buffer_wbl2 sc1
.Lfa_8:
	buffer_inv sc1
	s_add_i32 s76, s8, 0x900
	s_lshl_b64 s[6:7], s[76:77], 2
	v_readlane_b32 s10, v254, 46
	v_readlane_b32 s11, v254, 47
	s_add_u32 s14, s10, s6
	s_addc_u32 s15, s11, s7
	s_waitcnt lgkmcnt(0)
	global_load_dword v2, v1, s[14:15] sc1
	s_waitcnt vmcnt(0)
	v_cmp_eq_u32_e32 vcc, v2, v0
	s_and_saveexec_b64 s[6:7], vcc
	s_cbranch_execz .LBB0_641
	s_mov_b32 s9, 1
	s_mov_b64 s[16:17], 0
	s_branch .LBB0_632

.LBB0_794:
	s_or_b64 exec, exec, s[10:11]
	v_cvt_f32_u32_e32 v5, v3
	s_waitcnt vmcnt(0)
	v_readfirstlane_b32 s6, v4
	v_sub_u32_e32 v4, 0, v3
	v_rcp_iflag_f32_e32 v5, v5
	v_add_u32_e32 v6, s6, v0
	v_mul_f32_e32 v5, 0x4f7ffffe, v5
	v_cvt_u32_f32_e32 v5, v5
	v_mul_lo_u32 v0, v4, v5
	v_mul_hi_u32 v0, v5, v0
	v_add_u32_e32 v0, v5, v0
	v_mul_hi_u32 v0, v6, v0
	v_mul_lo_u32 v4, v0, v3
	v_sub_u32_e32 v4, v6, v4
	v_add_u32_e32 v5, 1, v0
	v_cmp_ge_u32_e32 vcc, v4, v3
	s_nop 1
	v_cndmask_b32_e32 v0, v0, v5, vcc
	v_sub_u32_e32 v5, v4, v3
	v_cndmask_b32_e32 v4, v4, v5, vcc
	v_add_u32_e32 v5, 1, v0
	v_cmp_ge_u32_e32 vcc, v4, v3
	v_add_u32_e32 v4, 1, v6
	s_nop 0
	v_cndmask_b32_e32 v0, v0, v5, vcc
	v_mul_lo_u32 v5, v3, v0
	v_add_u32_e32 v3, v5, v3
	v_cmp_ne_u32_e32 vcc, v4, v3
	s_and_saveexec_b64 s[6:7], vcc
	s_xor_b64 s[6:7], exec, s[6:7]
	s_cbranch_execz .LBB0_808
	v_cmp_eq_u32_e32 vcc, v6, v5
	s_cbranch_vccz .Lfa_12
	buffer_wbl2 sc1
.Lfa_12:
	buffer_inv sc1
	s_add_i32 s76, s8, 0x900
	s_lshl_b64 s[10:11], s[76:77], 2
	v_readlane_b32 s12, v254, 46
	v_readlane_b32 s13, v254, 47
	s_add_u32 s12, s12, s10
	s_addc_u32 s13, s13, s11
	s_waitcnt lgkmcnt(0)
	s_nop 1
	global_load_dword v2, v1, s[12:13] sc1
	s_waitcnt vmcnt(0)
	v_cmp_eq_u32_e32 vcc, v2, v0
	s_and_saveexec_b64 s[10:11], vcc
	s_cbranch_execz .LBB0_807
	s_mov_b32 s9, 1
	s_mov_b64 s[14:15], 0
	s_branch .LBB0_798

.LBB0_897:
	s_or_b64 exec, exec, s[4:5]
	v_cvt_f32_u32_e32 v5, v3
	s_waitcnt vmcnt(0)
	v_readfirstlane_b32 s2, v4
	v_sub_u32_e32 v4, 0, v3
	v_rcp_iflag_f32_e32 v5, v5
	v_add_u32_e32 v6, s2, v0
	v_mul_f32_e32 v5, 0x4f7ffffe, v5
	v_cvt_u32_f32_e32 v5, v5
	v_mul_lo_u32 v0, v4, v5
	v_mul_hi_u32 v0, v5, v0
	v_add_u32_e32 v0, v5, v0
	v_mul_hi_u32 v0, v6, v0
	v_mul_lo_u32 v4, v0, v3
	v_sub_u32_e32 v4, v6, v4
	v_add_u32_e32 v5, 1, v0
	v_cmp_ge_u32_e32 vcc, v4, v3
	s_nop 1
	v_cndmask_b32_e32 v0, v0, v5, vcc
	v_sub_u32_e32 v5, v4, v3
	v_cndmask_b32_e32 v4, v4, v5, vcc
	v_add_u32_e32 v5, 1, v0
	v_cmp_ge_u32_e32 vcc, v4, v3
	v_add_u32_e32 v4, 1, v6
	s_nop 0
	v_cndmask_b32_e32 v0, v0, v5, vcc
	v_mul_lo_u32 v5, v3, v0
	v_add_u32_e32 v3, v5, v3
	v_cmp_ne_u32_e32 vcc, v4, v3
	s_and_saveexec_b64 s[2:3], vcc
	s_xor_b64 s[2:3], exec, s[2:3]
	s_cbranch_execz .LBB0_911
	v_cmp_eq_u32_e32 vcc, v6, v5
	s_cbranch_vccz .Lfa_16
	buffer_wbl2 sc1
.Lfa_16:
	buffer_inv sc1
	s_add_i32 s76, s20, 0x900
	s_lshl_b64 s[4:5], s[76:77], 2
	v_readlane_b32 s6, v254, 46
	v_readlane_b32 s7, v254, 47
	s_add_u32 s6, s6, s4
	s_addc_u32 s7, s7, s5
	s_waitcnt lgkmcnt(0)
	s_nop 1
	global_load_dword v2, v1, s[6:7] sc1
	s_waitcnt vmcnt(0)
	v_cmp_eq_u32_e32 vcc, v2, v0
	s_and_saveexec_b64 s[4:5], vcc
	s_cbranch_execz .LBB0_910
	s_mov_b32 s18, 1
	s_mov_b64 s[8:9], 0
	s_branch .LBB0_901

.Lfa_20:
	buffer_inv sc1
	s_add_i32 s76, s23, 0x900
	s_lshl_b64 s[6:7], s[76:77], 2
	v_readlane_b32 s8, v254, 46
	v_readlane_b32 s9, v254, 47
	s_add_u32 s8, s8, s6
	s_addc_u32 s9, s9, s7
	s_waitcnt lgkmcnt(0)
	s_nop 1
	global_load_dword v2, v1, s[8:9] sc1
	s_waitcnt vmcnt(0)
	v_cmp_eq_u32_e32 vcc, v2, v0
	s_and_saveexec_b64 s[6:7], vcc
	s_cbranch_execz .LBB0_1110
	s_mov_b32 s20, 1
	s_mov_b64 s[10:11], 0
	s_branch .LBB0_1101

.Lfa_24:
	buffer_inv sc1
	s_add_i32 s76, s22, 0x900
	s_lshl_b64 s[6:7], s[76:77], 2
	v_readlane_b32 s8, v254, 46
	v_readlane_b32 s9, v254, 47
	s_add_u32 s8, s8, s6
	s_addc_u32 s9, s9, s7
	s_waitcnt lgkmcnt(0)
	s_nop 1
	global_load_dword v2, v1, s[8:9] sc1
	s_waitcnt vmcnt(0)
	v_cmp_eq_u32_e32 vcc, v2, v0
	s_and_saveexec_b64 s[6:7], vcc
	s_cbranch_execz .LBB0_1197
	s_mov_b32 s20, 1
	s_mov_b64 s[10:11], 0
	s_branch .LBB0_1188
